# v051
# baseline (speedup 1.0000x reference)
.Lgru_loop_a:
	v_mad_u32_u24 v227, v177, s17, v226
	s_nop 0
	s_waitcnt vmcnt(4)
	v_mfma_f32_16x16x32_f16 v[92:95], v[112:115], v[206:209], v[92:95]
	v_exp_f32_e32 v228, v144
	v_exp_f32_e32 v229, v145
	v_exp_f32_e32 v230, v146
	v_exp_f32_e32 v231, v147
	v_exp_f32_e32 v232, v148
	v_exp_f32_e32 v233, v149
	v_exp_f32_e32 v234, v150
	v_exp_f32_e32 v235, v151
	v_mfma_f32_16x16x32_f16 v[92:95], v[108:111], v[210:213], v[92:95]
	v_add_f32_e32 v228, 1.0, v228
	v_add_f32_e32 v229, 1.0, v229
	v_add_f32_e32 v230, 1.0, v230
	v_add_f32_e32 v231, 1.0, v231
	v_add_f32_e32 v232, 1.0, v232
	v_add_f32_e32 v233, 1.0, v233
	v_add_f32_e32 v234, 1.0, v234
	v_add_f32_e32 v235, 1.0, v235
	v_rcp_f32_e32 v228, v228
	v_rcp_f32_e32 v229, v229
	v_rcp_f32_e32 v230, v230
	v_rcp_f32_e32 v231, v231
	v_mfma_f32_16x16x32_f16 v[92:95], v[104:107], v[214:217], v[92:95]
	v_fma_f32 v236, v228, v152, v182
	v_fma_f32 v237, v229, v153, v183
	v_fma_f32 v238, v230, v154, v184
	v_fma_f32 v239, v231, v155, v185
	ds_read_b128 v[222:225], v227 offset:24848
	ds_read_b128 v[186:189], v227 offset:24864
	ds_read_b128 v[182:185], v227 offset:24880
	ds_read_u16 v177, v176 offset:4162
	v_exp_f32_e32 v236, v236
	v_exp_f32_e32 v237, v237
	v_exp_f32_e32 v238, v238
	v_exp_f32_e32 v239, v239
	v_rcp_f32_e32 v232, v232
	v_rcp_f32_e32 v233, v233
	v_mfma_f32_16x16x32_f16 v[92:95], v[100:103], v[218:221], v[92:95]
	global_load_dwordx4 v[112:115], v[166:167], off offset:-2048
	global_load_dwordx4 v[108:111], v[166:167], off offset:-1024
	global_load_dwordx4 v[104:107], v[166:167], off
	global_load_dwordx4 v[100:103], v[166:167], off offset:1024
	v_rcp_f32_e32 v234, v234
	v_rcp_f32_e32 v235, v235
	v_add_f32_e32 v236, 1.0, v236
	v_add_f32_e32 v237, 1.0, v237
	v_add_f32_e32 v238, 1.0, v238
	v_add_f32_e32 v239, 1.0, v239
	v_rcp_f32_e32 v236, v236
	v_rcp_f32_e32 v237, v237
	v_rcp_f32_e32 v238, v238
	v_rcp_f32_e32 v239, v239
	v_pk_fma_f32 v[236:237], v[236:237], -2.0, 1.0 op_sel_hi:[1,0,0]
	v_pk_fma_f32 v[238:239], v[238:239], -2.0, 1.0 op_sel_hi:[1,0,0]
	v_pk_add_f32 v[240:241], v[168:169], v[236:237] neg_lo:[0,1] neg_hi:[0,1]
	v_pk_add_f32 v[242:243], v[170:171], v[238:239] neg_lo:[0,1] neg_hi:[0,1]
	v_pk_fma_f32 v[168:169], v[232:233], v[240:241], v[236:237]
	v_pk_fma_f32 v[170:171], v[234:235], v[242:243], v[238:239]
	v_cvt_pk_f16_f32 v244, v168, v169
	v_cvt_pk_f16_f32 v245, v170, v171
	ds_read_b128 v[190:193], v156 offset:0
	ds_read_b128 v[194:197], v156 offset:1024
	ds_read_b128 v[198:201], v156 offset:2048
	ds_read_b128 v[202:205], v156 offset:3072
	ds_write_b64 v163, v[244:245] offset:4096
	s_waitcnt lgkmcnt(4)
	v_mfma_f32_16x16x32_f16 v[124:127], v[12:15], v[190:193], v[116:119]
	v_mfma_f32_16x16x32_f16 v[128:131], v[28:31], v[190:193], v[120:123]
	v_mfma_f32_16x16x32_f16 v[132:135], v[32:35], v[190:193], v[80:83]
	s_waitcnt lgkmcnt(3)
	v_mfma_f32_16x16x32_f16 v[124:127], v[16:19], v[194:197], v[124:127]
	v_mfma_f32_16x16x32_f16 v[128:131], v[48:51], v[194:197], v[128:131]
	v_mfma_f32_16x16x32_f16 v[132:135], v[36:39], v[194:197], v[132:135]
	s_waitcnt lgkmcnt(2)
	v_mfma_f32_16x16x32_f16 v[124:127], v[20:23], v[198:201], v[124:127]
	v_mfma_f32_16x16x32_f16 v[128:131], v[52:55], v[198:201], v[128:131]
	v_mfma_f32_16x16x32_f16 v[132:135], v[40:43], v[198:201], v[132:135]
	s_waitcnt lgkmcnt(1)
	v_mfma_f32_16x16x32_f16 v[124:127], v[24:27], v[202:205], v[124:127]
	v_mfma_f32_16x16x32_f16 v[128:131], v[56:59], v[202:205], v[128:131]
	v_mfma_f32_16x16x32_f16 v[132:135], v[44:47], v[202:205], v[132:135]
	s_waitcnt lgkmcnt(0)
	s_barrier
	v_mad_u32_u24 v227, v178, s17, v226
	s_nop 0
	s_waitcnt vmcnt(4)
	v_mfma_f32_16x16x32_f16 v[96:99], v[72:75], v[190:193], v[96:99]
	v_exp_f32_e32 v228, v124
	v_exp_f32_e32 v229, v125
	v_exp_f32_e32 v230, v126
	v_exp_f32_e32 v231, v127
	v_exp_f32_e32 v232, v128
	v_exp_f32_e32 v233, v129
	v_exp_f32_e32 v234, v130
	v_exp_f32_e32 v235, v131
	v_mfma_f32_16x16x32_f16 v[96:99], v[8:11], v[194:197], v[96:99]
	v_add_f32_e32 v228, 1.0, v228
	v_add_f32_e32 v229, 1.0, v229
	v_add_f32_e32 v230, 1.0, v230
	v_add_f32_e32 v231, 1.0, v231
	v_add_f32_e32 v232, 1.0, v232
	v_add_f32_e32 v233, 1.0, v233
	v_add_f32_e32 v234, 1.0, v234
	v_add_f32_e32 v235, 1.0, v235
	v_rcp_f32_e32 v228, v228
	v_rcp_f32_e32 v229, v229
	v_rcp_f32_e32 v230, v230
	v_rcp_f32_e32 v231, v231
	v_mfma_f32_16x16x32_f16 v[96:99], v[4:7], v[198:201], v[96:99]
	v_fma_f32 v236, v228, v132, v138
	v_fma_f32 v237, v229, v133, v139
	v_fma_f32 v238, v230, v134, v140
	v_fma_f32 v239, v231, v135, v141
	ds_read_b128 v[116:119], v227 offset:24848
	ds_read_b128 v[120:123], v227 offset:24864
	ds_read_b128 v[138:141], v227 offset:24880
	ds_read_u16 v178, v176 offset:4
	v_exp_f32_e32 v236, v236
	v_exp_f32_e32 v237, v237
	v_exp_f32_e32 v238, v238
	v_exp_f32_e32 v239, v239
	v_rcp_f32_e32 v232, v232
	v_rcp_f32_e32 v233, v233
	v_mfma_f32_16x16x32_f16 v[96:99], v[0:3], v[202:205], v[96:99]
	v_rcp_f32_e32 v234, v234
	v_rcp_f32_e32 v235, v235
	v_add_f32_e32 v236, 1.0, v236
	v_add_f32_e32 v237, 1.0, v237
	v_add_f32_e32 v238, 1.0, v238
	v_add_f32_e32 v239, 1.0, v239
	v_rcp_f32_e32 v236, v236
	v_rcp_f32_e32 v237, v237
	v_rcp_f32_e32 v238, v238
	v_rcp_f32_e32 v239, v239
	v_pk_fma_f32 v[236:237], v[236:237], -2.0, 1.0 op_sel_hi:[1,0,0]
	v_pk_fma_f32 v[238:239], v[238:239], -2.0, 1.0 op_sel_hi:[1,0,0]
	v_pk_add_f32 v[240:241], v[172:173], v[236:237] neg_lo:[0,1] neg_hi:[0,1]
	v_pk_add_f32 v[242:243], v[174:175], v[238:239] neg_lo:[0,1] neg_hi:[0,1]
	v_pk_fma_f32 v[172:173], v[232:233], v[240:241], v[236:237]
	v_pk_fma_f32 v[174:175], v[234:235], v[242:243], v[238:239]
	v_cvt_pk_f16_f32 v244, v172, v173
	v_cvt_pk_f16_f32 v245, v174, v175
	ds_read_b128 v[206:209], v156 offset:4096
	ds_read_b128 v[210:213], v156 offset:5120
	ds_read_b128 v[214:217], v156 offset:6144
	ds_read_b128 v[218:221], v156 offset:7168
	ds_write_b64 v163, v[244:245]
	s_waitcnt lgkmcnt(4)
	v_mfma_f32_16x16x32_f16 v[144:147], v[12:15], v[206:209], v[222:225]
	v_mfma_f32_16x16x32_f16 v[148:151], v[28:31], v[206:209], v[186:189]
	v_mfma_f32_16x16x32_f16 v[152:155], v[32:35], v[206:209], v[80:83]
	s_waitcnt lgkmcnt(3)
	v_mfma_f32_16x16x32_f16 v[144:147], v[16:19], v[210:213], v[144:147]
	v_mfma_f32_16x16x32_f16 v[148:151], v[48:51], v[210:213], v[148:151]
	v_mfma_f32_16x16x32_f16 v[152:155], v[36:39], v[210:213], v[152:155]
	s_waitcnt lgkmcnt(2)
	v_mfma_f32_16x16x32_f16 v[144:147], v[20:23], v[214:217], v[144:147]
	v_mfma_f32_16x16x32_f16 v[148:151], v[52:55], v[214:217], v[148:151]
	v_mfma_f32_16x16x32_f16 v[152:155], v[40:43], v[214:217], v[152:155]
	s_waitcnt lgkmcnt(1)
	v_mfma_f32_16x16x32_f16 v[144:147], v[24:27], v[218:221], v[144:147]
	v_mfma_f32_16x16x32_f16 v[148:151], v[56:59], v[218:221], v[148:151]
	v_mfma_f32_16x16x32_f16 v[152:155], v[44:47], v[218:221], v[152:155]
	s_waitcnt lgkmcnt(0)
	s_barrier
	v_mad_u32_u24 v227, v177, s17, v226
	s_nop 0
	s_waitcnt vmcnt(4)
	v_mfma_f32_16x16x32_f16 v[92:95], v[72:75], v[206:209], v[92:95]
	v_exp_f32_e32 v228, v144
	v_exp_f32_e32 v229, v145
	v_exp_f32_e32 v230, v146
	v_exp_f32_e32 v231, v147
	v_exp_f32_e32 v232, v148
	v_exp_f32_e32 v233, v149
	v_exp_f32_e32 v234, v150
	v_exp_f32_e32 v235, v151
	v_mfma_f32_16x16x32_f16 v[92:95], v[8:11], v[210:213], v[92:95]
	v_add_f32_e32 v228, 1.0, v228
	v_add_f32_e32 v229, 1.0, v229
	v_add_f32_e32 v230, 1.0, v230
	v_add_f32_e32 v231, 1.0, v231
	v_add_f32_e32 v232, 1.0, v232
	v_add_f32_e32 v233, 1.0, v233
	v_add_f32_e32 v234, 1.0, v234
	v_add_f32_e32 v235, 1.0, v235
	v_rcp_f32_e32 v228, v228
	v_rcp_f32_e32 v229, v229
	v_rcp_f32_e32 v230, v230
	v_rcp_f32_e32 v231, v231
	v_mfma_f32_16x16x32_f16 v[92:95], v[4:7], v[214:217], v[92:95]
	v_fma_f32 v236, v228, v152, v182
	v_fma_f32 v237, v229, v153, v183
	v_fma_f32 v238, v230, v154, v184
	v_fma_f32 v239, v231, v155, v185
	ds_read_b128 v[222:225], v227 offset:24848
	ds_read_b128 v[186:189], v227 offset:24864
	ds_read_b128 v[182:185], v227 offset:24880
	ds_read_u16 v177, v176 offset:4164
	v_exp_f32_e32 v236, v236
	v_exp_f32_e32 v237, v237
	v_exp_f32_e32 v238, v238
	v_exp_f32_e32 v239, v239
	v_rcp_f32_e32 v232, v232
	v_rcp_f32_e32 v233, v233
	v_mfma_f32_16x16x32_f16 v[92:95], v[0:3], v[218:221], v[92:95]
	s_ashr_i32 s9, s8, 31
	s_lshl_b64 s[12:13], s[8:9], 15
	v_lshl_add_u64 v[246:247], v[158:159], 0, s[12:13]
	global_load_dwordx4 v[72:75], v[246:247], off
	global_load_dwordx4 v[8:11], v[246:247], off offset:1024
	global_load_dwordx4 v[4:7], v[246:247], off offset:2048
	global_load_dwordx4 v[0:3], v[246:247], off offset:3072
	v_rcp_f32_e32 v234, v234
	v_rcp_f32_e32 v235, v235
	v_add_f32_e32 v236, 1.0, v236
	v_add_f32_e32 v237, 1.0, v237
	v_add_f32_e32 v238, 1.0, v238
	v_add_f32_e32 v239, 1.0, v239
	v_rcp_f32_e32 v236, v236
	v_rcp_f32_e32 v237, v237
	v_rcp_f32_e32 v238, v238
	v_rcp_f32_e32 v239, v239
	v_pk_fma_f32 v[236:237], v[236:237], -2.0, 1.0 op_sel_hi:[1,0,0]
	v_pk_fma_f32 v[238:239], v[238:239], -2.0, 1.0 op_sel_hi:[1,0,0]
	v_pk_add_f32 v[240:241], v[168:169], v[236:237] neg_lo:[0,1] neg_hi:[0,1]
	v_pk_add_f32 v[242:243], v[170:171], v[238:239] neg_lo:[0,1] neg_hi:[0,1]
	v_pk_fma_f32 v[168:169], v[232:233], v[240:241], v[236:237]
	v_pk_fma_f32 v[170:171], v[234:235], v[242:243], v[238:239]
	v_cvt_pk_f16_f32 v244, v168, v169
	v_cvt_pk_f16_f32 v245, v170, v171
	ds_read_b128 v[190:193], v156 offset:0
	ds_read_b128 v[194:197], v156 offset:1024
	ds_read_b128 v[198:201], v156 offset:2048
	ds_read_b128 v[202:205], v156 offset:3072
	ds_write_b64 v163, v[244:245] offset:4096
	s_waitcnt lgkmcnt(4)
	v_mfma_f32_16x16x32_f16 v[124:127], v[12:15], v[190:193], v[116:119]
	v_mfma_f32_16x16x32_f16 v[128:131], v[28:31], v[190:193], v[120:123]
	v_mfma_f32_16x16x32_f16 v[132:135], v[32:35], v[190:193], v[80:83]
	s_waitcnt lgkmcnt(3)
	v_mfma_f32_16x16x32_f16 v[124:127], v[16:19], v[194:197], v[124:127]
	v_mfma_f32_16x16x32_f16 v[128:131], v[48:51], v[194:197], v[128:131]
	v_mfma_f32_16x16x32_f16 v[132:135], v[36:39], v[194:197], v[132:135]
	s_waitcnt lgkmcnt(2)
	v_mfma_f32_16x16x32_f16 v[124:127], v[20:23], v[198:201], v[124:127]
	v_mfma_f32_16x16x32_f16 v[128:131], v[52:55], v[198:201], v[128:131]
	v_mfma_f32_16x16x32_f16 v[132:135], v[40:43], v[198:201], v[132:135]
	s_waitcnt lgkmcnt(1)
	v_mfma_f32_16x16x32_f16 v[124:127], v[24:27], v[202:205], v[124:127]
	v_mfma_f32_16x16x32_f16 v[128:131], v[56:59], v[202:205], v[128:131]
	v_mfma_f32_16x16x32_f16 v[132:135], v[44:47], v[202:205], v[132:135]
	s_waitcnt lgkmcnt(0)
	s_barrier
	v_mad_u32_u24 v227, v178, s17, v226
	s_nop 0
	s_waitcnt vmcnt(4)
	v_mfma_f32_16x16x32_f16 v[96:99], v[112:115], v[190:193], v[96:99]
	v_exp_f32_e32 v228, v124
	v_exp_f32_e32 v229, v125
	v_exp_f32_e32 v230, v126
	v_exp_f32_e32 v231, v127
	v_exp_f32_e32 v232, v128
	v_exp_f32_e32 v233, v129
	v_exp_f32_e32 v234, v130
	v_exp_f32_e32 v235, v131
	v_mfma_f32_16x16x32_f16 v[96:99], v[108:111], v[194:197], v[96:99]
	v_add_f32_e32 v228, 1.0, v228
	v_add_f32_e32 v229, 1.0, v229
	v_add_f32_e32 v230, 1.0, v230
	v_add_f32_e32 v231, 1.0, v231
	v_add_f32_e32 v232, 1.0, v232
	v_add_f32_e32 v233, 1.0, v233
	v_add_f32_e32 v234, 1.0, v234
	v_add_f32_e32 v235, 1.0, v235
	v_rcp_f32_e32 v228, v228
	v_rcp_f32_e32 v229, v229
	v_rcp_f32_e32 v230, v230
	v_rcp_f32_e32 v231, v231
	v_mfma_f32_16x16x32_f16 v[96:99], v[104:107], v[198:201], v[96:99]
	v_fma_f32 v236, v228, v132, v138
	v_fma_f32 v237, v229, v133, v139
	v_fma_f32 v238, v230, v134, v140
	v_fma_f32 v239, v231, v135, v141
	ds_read_b128 v[116:119], v227 offset:24848
	ds_read_b128 v[120:123], v227 offset:24864
	ds_read_b128 v[138:141], v227 offset:24880
	ds_read_u16 v178, v176 offset:6
	v_exp_f32_e32 v236, v236
	v_exp_f32_e32 v237, v237
	v_exp_f32_e32 v238, v238
	v_exp_f32_e32 v239, v239
	v_rcp_f32_e32 v232, v232
	v_rcp_f32_e32 v233, v233
	v_mfma_f32_16x16x32_f16 v[96:99], v[100:103], v[202:205], v[96:99]
	v_rcp_f32_e32 v234, v234
	v_rcp_f32_e32 v235, v235
	v_add_f32_e32 v236, 1.0, v236
	v_add_f32_e32 v237, 1.0, v237
	v_add_f32_e32 v238, 1.0, v238
	v_add_f32_e32 v239, 1.0, v239
	v_rcp_f32_e32 v236, v236
	v_rcp_f32_e32 v237, v237
	v_rcp_f32_e32 v238, v238
	v_rcp_f32_e32 v239, v239
	v_pk_fma_f32 v[236:237], v[236:237], -2.0, 1.0 op_sel_hi:[1,0,0]
	v_pk_fma_f32 v[238:239], v[238:239], -2.0, 1.0 op_sel_hi:[1,0,0]
	v_pk_add_f32 v[240:241], v[172:173], v[236:237] neg_lo:[0,1] neg_hi:[0,1]
	v_pk_add_f32 v[242:243], v[174:175], v[238:239] neg_lo:[0,1] neg_hi:[0,1]
	v_pk_fma_f32 v[172:173], v[232:233], v[240:241], v[236:237]
	v_pk_fma_f32 v[174:175], v[234:235], v[242:243], v[238:239]
	v_cvt_pk_f16_f32 v244, v172, v173
	v_cvt_pk_f16_f32 v245, v174, v175
	ds_read_b128 v[206:209], v156 offset:4096
	ds_read_b128 v[210:213], v156 offset:5120
	ds_read_b128 v[214:217], v156 offset:6144
	ds_read_b128 v[218:221], v156 offset:7168
	ds_write_b64 v163, v[244:245]
	s_waitcnt lgkmcnt(4)
	v_mfma_f32_16x16x32_f16 v[144:147], v[12:15], v[206:209], v[222:225]
	v_mfma_f32_16x16x32_f16 v[148:151], v[28:31], v[206:209], v[186:189]
	v_mfma_f32_16x16x32_f16 v[152:155], v[32:35], v[206:209], v[80:83]
	s_waitcnt lgkmcnt(3)
	v_mfma_f32_16x16x32_f16 v[144:147], v[16:19], v[210:213], v[144:147]
	v_mfma_f32_16x16x32_f16 v[148:151], v[48:51], v[210:213], v[148:151]
	v_mfma_f32_16x16x32_f16 v[152:155], v[36:39], v[210:213], v[152:155]
	s_waitcnt lgkmcnt(2)
	v_mfma_f32_16x16x32_f16 v[144:147], v[20:23], v[214:217], v[144:147]
	v_mfma_f32_16x16x32_f16 v[148:151], v[52:55], v[214:217], v[148:151]
	v_mfma_f32_16x16x32_f16 v[152:155], v[40:43], v[214:217], v[152:155]
	s_waitcnt lgkmcnt(1)
	v_mfma_f32_16x16x32_f16 v[144:147], v[24:27], v[218:221], v[144:147]
	v_mfma_f32_16x16x32_f16 v[148:151], v[56:59], v[218:221], v[148:151]
	v_mfma_f32_16x16x32_f16 v[152:155], v[44:47], v[218:221], v[152:155]
	s_add_i32 s5, s5, 2
	s_add_i32 s8, s8, s4
	v_add_u32_e32 v176, 4, v176
	v_lshl_add_u64 v[166:167], v[166:167], 0, s[6:7]
	s_cmpk_gt_u32 s5, 0x7d
	s_waitcnt lgkmcnt(0)
	s_barrier
	s_cbranch_scc0 .Lgru_loop_a
	s_branch .Lgru_tail
